# P6 two-sweep loops: descriptor, row-id and gate-operand LDS reads of an iteration issued together ahead of one wait (one LDS round trip per visit instead of three)
# speedup vs baseline: 1.0318x; 1.0102x over previous
.LBB0_950:
	s_or_b64 exec, exec, s[0:1]
	s_waitcnt vmcnt(0)
	v_mov_b32_e32 v1, s85
	ds_read_b32 v1, v1 offset:4864
	s_or_b32 s96, s2, s33
	s_ashr_i32 s97, s96, 31
	v_readlane_b32 s22, v9, 63
	s_waitcnt lgkmcnt(0)
	v_readfirstlane_b32 s26, v1
	s_and_b32 s0, s26, 0x3ff
	s_bfe_u32 s1, s26, 0x4000a
	v_cmp_gt_u32_e32 vcc, s1, v182
	s_lshl_b32 s0, s0, 2
	s_add_i32 s0, s0, s85
	v_cndmask_b32_e32 v1, 0, v182, vcc
	v_lshl_add_u32 v1, v1, 2, s0
	ds_read_b32 v1, v1 offset:8192
	s_lshl_b64 s[0:1], s[96:97], 11
	s_lshr_b32 s23, s26, 3
	v_lshl_add_u64 v[142:143], v[76:77], 0, s[0:1]
	s_and_b32 s88, s23, 0x1ffff800
	s_waitcnt lgkmcnt(0)
	v_lshlrev_b32_e32 v1, 10, v1
	v_and_b32_e32 v1, 0x3fffc00, v1
	v_lshl_add_u64 v[12:13], v[142:143], 0, s[88:89]
	global_load_dwordx4 v[8:11], v[12:13], off
	global_load_dwordx4 v[4:7], v[12:13], off offset:16
	v_readlane_b32 s0, v1, 0
	v_readlane_b32 s1, v1, 1
	v_readlane_b32 s2, v1, 2
	v_readlane_b32 s3, v1, 3
	v_readlane_b32 s14, v1, 4
	v_readlane_b32 s15, v1, 5
	v_readlane_b32 s20, v1, 6
	v_readlane_b32 s21, v1, 7
	s_nop 4
	buffer_load_dwordx4 v[68:71], v181, s[8:11], s0 offen
	buffer_load_dwordx4 v[64:67], v181, s[8:11], s1 offen
	buffer_load_dwordx4 v[60:63], v181, s[8:11], s2 offen
	buffer_load_dwordx4 v[56:59], v181, s[8:11], s3 offen
	buffer_load_dwordx4 v[48:51], v181, s[8:11], s14 offen
	buffer_load_dwordx4 v[32:35], v181, s[8:11], s15 offen
	buffer_load_dwordx4 v[16:19], v181, s[8:11], s20 offen
	buffer_load_dwordx4 v[12:15], v181, s[8:11], s21 offen
	s_add_i32 s3, s22, -1
	s_min_i32 s2, s3, 1
	s_max_i32 s2, s2, 0
	s_lshl_b32 s2, s2, 2
	s_add_i32 s2, s85, s2
	v_mov_b32_e32 v1, s2
	ds_read_b32 v1, v1 offset:4864
	s_waitcnt lgkmcnt(0)
	v_readfirstlane_b32 s86, v1
	s_and_b32 s2, s86, 0x3ff
	s_bfe_u32 s3, s86, 0x4000a
	v_cmp_gt_u32_e32 vcc, s3, v182
	s_lshl_b32 s2, s2, 2
	s_add_i32 s2, s2, s85
	v_cndmask_b32_e32 v1, 0, v182, vcc
	v_lshl_add_u32 v1, v1, 2, s2
	ds_read_b32 v1, v1 offset:8192
	s_waitcnt lgkmcnt(0)
	v_lshlrev_b32_e32 v1, 10, v1
	v_and_b32_e32 v1, 0x3fffc00, v1
	s_nop 0
	v_readlane_b32 s44, v1, 0
	v_readlane_b32 s45, v1, 1
	v_readlane_b32 s46, v1, 2
	v_readlane_b32 s47, v1, 3
	v_readlane_b32 s48, v1, 4
	v_readlane_b32 s49, v1, 5
	v_readlane_b32 s50, v1, 6
	v_readlane_b32 s51, v1, 7
	s_nop 4
	buffer_load_dwordx4 v[72:75], v181, s[8:11], s44 offen
	buffer_load_dwordx4 v[52:55], v181, s[8:11], s45 offen
	buffer_load_dwordx4 v[44:47], v181, s[8:11], s46 offen
	buffer_load_dwordx4 v[40:43], v181, s[8:11], s47 offen
	buffer_load_dwordx4 v[36:39], v181, s[8:11], s48 offen
	buffer_load_dwordx4 v[28:31], v181, s[8:11], s49 offen
	buffer_load_dwordx4 v[24:27], v181, s[8:11], s50 offen
	buffer_load_dwordx4 v[20:23], v181, s[8:11], s51 offen
	s_add_i32 s3, s22, -1
	s_min_i32 s2, s3, 2
	s_max_i32 s2, s2, 0
	s_lshl_b32 s2, s2, 2
	s_add_i32 s2, s85, s2
	v_mov_b32_e32 v1, s2
	ds_read_b32 v1, v1 offset:4864
	s_waitcnt lgkmcnt(0)
	v_readfirstlane_b32 s27, v1
	s_and_b32 s2, s27, 0x3ff
	s_bfe_u32 s3, s27, 0x4000a
	v_cmp_gt_u32_e32 vcc, s3, v182
	s_lshl_b32 s2, s2, 2
	s_add_i32 s2, s2, s85
	v_cndmask_b32_e32 v1, 0, v182, vcc
	v_lshl_add_u32 v1, v1, 2, s2
	ds_read_b32 v1, v1 offset:8192
	s_waitcnt lgkmcnt(0)
	v_lshlrev_b32_e32 v1, 10, v1
	v_and_b32_e32 v1, 0x3fffc00, v1
	s_nop 0
	v_readlane_b32 s44, v1, 0
	v_readlane_b32 s45, v1, 1
	v_readlane_b32 s46, v1, 2
	v_readlane_b32 s47, v1, 3
	v_readlane_b32 s48, v1, 4
	v_readlane_b32 s49, v1, 5
	v_readlane_b32 s50, v1, 6
	v_readlane_b32 s51, v1, 7
	s_nop 4
	buffer_load_dwordx4 v[224:227], v181, s[8:11], s44 offen
	buffer_load_dwordx4 v[228:231], v181, s[8:11], s45 offen
	buffer_load_dwordx4 v[232:235], v181, s[8:11], s46 offen
	buffer_load_dwordx4 v[236:239], v181, s[8:11], s47 offen
	buffer_load_dwordx4 v[240:243], v181, s[8:11], s48 offen
	buffer_load_dwordx4 v[244:247], v181, s[8:11], s49 offen
	buffer_load_dwordx4 v[248:251], v181, s[8:11], s50 offen
	buffer_load_dwordx4 v[216:219], v181, s[8:11], s51 offen
	s_add_i32 s3, s22, -1
	s_min_i32 s2, s3, 3
	s_max_i32 s2, s2, 0
	s_lshl_b32 s2, s2, 2
	s_add_i32 s2, s85, s2
	v_mov_b32_e32 v1, s2
	ds_read_b32 v1, v1 offset:4864
	s_waitcnt lgkmcnt(0)
	v_readfirstlane_b32 s32, v1
	s_cmp_lt_i32 s22, 1
	s_cbranch_scc1 .LBB0_974
	v_mov_b32_e32 v84, 0
	s_mov_b32 s23, 0
	s_mov_b64 s[0:1], -1
	v_mov_b32_e32 v158, 0
	v_mov_b32_e32 v159, 0
	v_mov_b32_e32 v156, 0
	v_mov_b32_e32 v157, 0
	v_mov_b32_e32 v154, 0
	v_mov_b32_e32 v155, 0
	v_mov_b32_e32 v152, 0
	v_mov_b32_e32 v153, 0
	v_mov_b32_e32 v150, 0
	v_mov_b32_e32 v151, 0
	v_mov_b32_e32 v148, 0
	v_mov_b32_e32 v149, 0
	v_mov_b32_e32 v146, 0
	v_mov_b32_e32 v147, 0
	v_mov_b32_e32 v144, 0
	v_mov_b32_e32 v145, 0
	v_mov_b32_e32 v85, v84
	v_mov_b32_e32 v92, v84
	v_mov_b32_e32 v93, v84
	v_mov_b32_e32 v90, v84
	v_mov_b32_e32 v91, v84
	v_mov_b32_e32 v88, v84
	v_mov_b32_e32 v89, v84
	v_mov_b32_e32 v86, v84
	v_mov_b32_e32 v87, v84
	v_mov_b32_e32 v82, v84
	v_mov_b32_e32 v83, v84
	v_mov_b32_e32 v80, v84
	v_mov_b32_e32 v81, v84
	v_mov_b32_e32 v78, v84
	v_mov_b32_e32 v79, v84
	v_mov_b32_e32 v108, v84
	v_mov_b32_e32 v109, v84
	v_mov_b32_e32 v106, v84
	v_mov_b32_e32 v107, v84
	v_mov_b32_e32 v104, v84
	v_mov_b32_e32 v105, v84
	v_mov_b32_e32 v102, v84
	v_mov_b32_e32 v103, v84
	v_mov_b32_e32 v100, v84
	v_mov_b32_e32 v101, v84
	v_mov_b32_e32 v98, v84
	v_mov_b32_e32 v99, v84
	v_mov_b32_e32 v96, v84
	v_mov_b32_e32 v97, v84
	v_mov_b32_e32 v94, v84
	v_mov_b32_e32 v95, v84
	v_mov_b32_e32 v124, v84
	v_mov_b32_e32 v125, v84
	v_mov_b32_e32 v122, v84
	v_mov_b32_e32 v123, v84
	v_mov_b32_e32 v120, v84
	v_mov_b32_e32 v121, v84
	v_mov_b32_e32 v118, v84
	v_mov_b32_e32 v119, v84
	v_mov_b32_e32 v116, v84
	v_mov_b32_e32 v117, v84
	v_mov_b32_e32 v114, v84
	v_mov_b32_e32 v115, v84
	v_mov_b32_e32 v112, v84
	v_mov_b32_e32 v113, v84
	v_mov_b32_e32 v110, v84
	v_mov_b32_e32 v111, v84
	v_mov_b32_e32 v140, v84
	v_mov_b32_e32 v141, v84
	v_mov_b32_e32 v138, v84
	v_mov_b32_e32 v139, v84
	v_mov_b32_e32 v136, v84
	v_mov_b32_e32 v137, v84
	v_mov_b32_e32 v134, v84
	v_mov_b32_e32 v135, v84
	v_mov_b32_e32 v132, v84
	v_mov_b32_e32 v133, v84
	v_mov_b32_e32 v130, v84
	v_mov_b32_e32 v131, v84
	v_mov_b32_e32 v128, v84
	v_mov_b32_e32 v129, v84
	v_mov_b32_e32 v126, v84
	v_mov_b32_e32 v127, v84
.Lp6a0_top:
	s_add_i32 s23, s23, 1
	s_add_i32 s2, s23, 3
	s_add_i32 s3, s22, -1
	s_min_i32 s2, s2, s3
	s_lshl_b32 s2, s2, 2
	s_add_i32 s2, s85, s2
	v_mov_b32_e32 v1, s2
	ds_read_b32 v252, v1 offset:4864
	s_and_b32 s2, s32, 0x3ff
	s_bfe_u32 s3, s32, 0x4000a
	v_cmp_gt_u32_e32 vcc, s3, v182
	s_lshl_b32 s2, s2, 2
	s_add_i32 s2, s2, s85
	v_cndmask_b32_e32 v1, 0, v182, vcc
	v_lshl_add_u32 v1, v1, 2, s2
	ds_read_b32 v1, v1 offset:8192
	s_and_b32 s2, s26, 0x3ff
	v_add_u32_e32 v210, s2, v180
	v_lshl_add_u32 v210, v210, 2, s85
	ds_read_b32 v196, v210
	ds_read_b32 v201, v210 offset:12288
	s_waitcnt vmcnt(16)
	s_andn2_b64 vcc, exec, s[0:1]
	s_waitcnt lgkmcnt(0)
	v_readfirstlane_b32 s37, v252
	v_lshlrev_b32_e32 v1, 10, v1
	v_and_b32_e32 v1, 0x3fffc00, v1
	s_nop 0
	v_readlane_b32 s44, v1, 0
	v_readlane_b32 s45, v1, 1
	v_readlane_b32 s46, v1, 2
	v_readlane_b32 s47, v1, 3
	v_readlane_b32 s48, v1, 4
	v_readlane_b32 s49, v1, 5
	v_readlane_b32 s50, v1, 6
	v_readlane_b32 s51, v1, 7
	s_cbranch_vccnz .Lp6a0_954
	s_waitcnt vmcnt(8)
	v_lshlrev_b32_e32 v144, 16, v8
	v_and_b32_e32 v145, 0xffff0000, v8
	v_lshlrev_b32_e32 v146, 16, v9
	v_and_b32_e32 v147, 0xffff0000, v9
	v_lshlrev_b32_e32 v148, 16, v10
	v_and_b32_e32 v149, 0xffff0000, v10
	v_lshlrev_b32_e32 v150, 16, v11
	v_and_b32_e32 v151, 0xffff0000, v11
	v_lshlrev_b32_e32 v152, 16, v4
	v_and_b32_e32 v153, 0xffff0000, v4
	v_lshlrev_b32_e32 v154, 16, v5
	v_and_b32_e32 v155, 0xffff0000, v5
	v_lshlrev_b32_e32 v156, 16, v6
	v_and_b32_e32 v157, 0xffff0000, v6
	v_lshlrev_b32_e32 v158, 16, v7
	v_and_b32_e32 v159, 0xffff0000, v7

.Lp6a0_dotdone:
	s_nop 4
	buffer_load_dwordx4 v[68:71], v181, s[8:11], s44 offen
	buffer_load_dwordx4 v[64:67], v181, s[8:11], s45 offen
	buffer_load_dwordx4 v[60:63], v181, s[8:11], s46 offen
	buffer_load_dwordx4 v[56:59], v181, s[8:11], s47 offen
	buffer_load_dwordx4 v[48:51], v181, s[8:11], s48 offen
	buffer_load_dwordx4 v[32:35], v181, s[8:11], s49 offen
	buffer_load_dwordx4 v[16:19], v181, s[8:11], s50 offen
	buffer_load_dwordx4 v[12:15], v181, s[8:11], s51 offen
	v_permlane32_swap_b32_e32 v160, v168
	v_permlane32_swap_b32_e32 v162, v170
	v_permlane32_swap_b32_e32 v164, v172
	v_permlane32_swap_b32_e32 v166, v174
	v_add_f32_e32 v1, v160, v168
	v_add_f32_e32 v2, v162, v170
	v_add_f32_e32 v160, v164, v172
	v_add_f32_e32 v161, v166, v174
	s_nop 0
	v_permlane16_swap_b32_e32 v1, v160
	v_permlane16_swap_b32_e32 v2, v161
	v_add_f32_e32 v1, v1, v160
	v_add_f32_e32 v2, v2, v161
	v_cndmask_b32_e64 v160, v1, v2, s[4:5]
	v_cndmask_b32_e64 v1, v2, v1, s[4:5]
	s_bfe_u32 s14, s26, 0x4000a
	v_cmp_gt_u32_e32 vcc, s14, v180
	v_add_f32_dpp v1, v160, v1 row_ror:8 row_mask:0xf bank_mask:0xf bound_ctrl:1
	s_nop 1
	v_add_f32_dpp v1, v1, v1 row_half_mirror row_mask:0xf bank_mask:0xf bound_ctrl:1
	s_nop 1
	v_add_f32_dpp v2, v1, v1 quad_perm:[1,0,3,2] row_mask:0xf bank_mask:0xf bound_ctrl:1
	v_mov_b32_e32 v1, 0
	s_nop 0
	v_mov_b32_dpp v160, v2 quad_perm:[2,3,0,1] row_mask:0xf bank_mask:0xf bound_ctrl:1
	s_and_saveexec_b64 s[14:15], vcc
	s_cbranch_execz .Lp6a0_958
	s_and_b32 s26, s26, 0x3ff
	v_add_u32_e32 v1, s26, v180
	v_lshl_add_u32 v1, v1, 2, s85
	v_add_f32_e32 v2, v2, v160
	s_mov_b32 s26, 0x3e6d3388
	v_mul_f32_e32 v1, v2, v196
	v_fma_f32 v2, |v1|, s26, 1.0
	v_rcp_f32_e32 v2, v2
	v_mov_b32_e32 v160, 0xbf3a00e3
	v_cmp_gt_f32_e32 vcc, 0, v1
	v_fmamk_f32 v160, v2, 0x3f07dc22, v160
	v_fmaak_f32 v160, v2, v160, 0x3f35f0e3
	v_fmaak_f32 v160, v2, v160, 0xbe11a98e
	v_fmaak_f32 v160, v2, v160, 0x3e027906
	v_mul_f32_e32 v2, v2, v160
	v_mul_f32_e32 v160, v1, v1
	v_mul_f32_e32 v160, 0xbf38aa3b, v160
	v_exp_f32_e32 v160, v160
	s_nop 0
	v_mul_f32_e32 v2, v160, v2
	v_mul_f32_e32 v160, v1, v2
	v_fma_f32 v1, -v1, v2, v1
	v_cndmask_b32_e32 v1, v1, v160, vcc
	v_mul_f32_e32 v1, v201, v1
	ds_write_b32 v210, v1 offset:12288
.Lp6a0_958:
	s_or_b64 exec, exec, s[14:15]
	s_mov_b32 s26, s86
	s_mov_b32 s86, s27
	s_mov_b32 s27, s32
	s_mov_b32 s32, s37
	s_cmp_eq_u32 s22, s23
	s_cbranch_scc1 .Lp6_Adone

.Lp6a1_dotdone:
	s_nop 4
	buffer_load_dwordx4 v[72:75], v181, s[8:11], s44 offen
	buffer_load_dwordx4 v[52:55], v181, s[8:11], s45 offen
	buffer_load_dwordx4 v[44:47], v181, s[8:11], s46 offen
	buffer_load_dwordx4 v[40:43], v181, s[8:11], s47 offen
	buffer_load_dwordx4 v[36:39], v181, s[8:11], s48 offen
	buffer_load_dwordx4 v[28:31], v181, s[8:11], s49 offen
	buffer_load_dwordx4 v[24:27], v181, s[8:11], s50 offen
	buffer_load_dwordx4 v[20:23], v181, s[8:11], s51 offen
	v_permlane32_swap_b32_e32 v160, v168
	v_permlane32_swap_b32_e32 v162, v170
	v_permlane32_swap_b32_e32 v164, v172
	v_permlane32_swap_b32_e32 v166, v174
	v_add_f32_e32 v1, v160, v168
	v_add_f32_e32 v2, v162, v170
	v_add_f32_e32 v160, v164, v172
	v_add_f32_e32 v161, v166, v174
	s_nop 0
	v_permlane16_swap_b32_e32 v1, v160
	v_permlane16_swap_b32_e32 v2, v161
	v_add_f32_e32 v1, v1, v160
	v_add_f32_e32 v2, v2, v161
	v_cndmask_b32_e64 v160, v1, v2, s[4:5]
	v_cndmask_b32_e64 v1, v2, v1, s[4:5]
	s_bfe_u32 s14, s26, 0x4000a
	v_cmp_gt_u32_e32 vcc, s14, v180
	v_add_f32_dpp v1, v160, v1 row_ror:8 row_mask:0xf bank_mask:0xf bound_ctrl:1
	s_nop 1
	v_add_f32_dpp v1, v1, v1 row_half_mirror row_mask:0xf bank_mask:0xf bound_ctrl:1
	s_nop 1
	v_add_f32_dpp v2, v1, v1 quad_perm:[1,0,3,2] row_mask:0xf bank_mask:0xf bound_ctrl:1
	v_mov_b32_e32 v1, 0
	s_nop 0
	v_mov_b32_dpp v160, v2 quad_perm:[2,3,0,1] row_mask:0xf bank_mask:0xf bound_ctrl:1
	s_and_saveexec_b64 s[14:15], vcc
	s_cbranch_execz .Lp6a1_958
	s_and_b32 s26, s26, 0x3ff
	v_add_u32_e32 v1, s26, v180
	v_lshl_add_u32 v1, v1, 2, s85
	v_add_f32_e32 v2, v2, v160
	s_mov_b32 s26, 0x3e6d3388
	v_mul_f32_e32 v1, v2, v196
	v_fma_f32 v2, |v1|, s26, 1.0
	v_rcp_f32_e32 v2, v2
	v_mov_b32_e32 v160, 0xbf3a00e3
	v_cmp_gt_f32_e32 vcc, 0, v1
	v_fmamk_f32 v160, v2, 0x3f07dc22, v160
	v_fmaak_f32 v160, v2, v160, 0x3f35f0e3
	v_fmaak_f32 v160, v2, v160, 0xbe11a98e
	v_fmaak_f32 v160, v2, v160, 0x3e027906
	v_mul_f32_e32 v2, v2, v160
	v_mul_f32_e32 v160, v1, v1
	v_mul_f32_e32 v160, 0xbf38aa3b, v160
	v_exp_f32_e32 v160, v160
	s_nop 0
	v_mul_f32_e32 v2, v160, v2
	v_mul_f32_e32 v160, v1, v2
	v_fma_f32 v1, -v1, v2, v1
	v_cndmask_b32_e32 v1, v1, v160, vcc
	v_mul_f32_e32 v1, v201, v1
	ds_write_b32 v210, v1 offset:12288

.Lp6a2_dotdone:
	s_nop 4
	buffer_load_dwordx4 v[224:227], v181, s[8:11], s44 offen
	buffer_load_dwordx4 v[228:231], v181, s[8:11], s45 offen
	buffer_load_dwordx4 v[232:235], v181, s[8:11], s46 offen
	buffer_load_dwordx4 v[236:239], v181, s[8:11], s47 offen
	buffer_load_dwordx4 v[240:243], v181, s[8:11], s48 offen
	buffer_load_dwordx4 v[244:247], v181, s[8:11], s49 offen
	buffer_load_dwordx4 v[248:251], v181, s[8:11], s50 offen
	buffer_load_dwordx4 v[216:219], v181, s[8:11], s51 offen
	v_permlane32_swap_b32_e32 v160, v168
	v_permlane32_swap_b32_e32 v162, v170
	v_permlane32_swap_b32_e32 v164, v172
	v_permlane32_swap_b32_e32 v166, v174
	v_add_f32_e32 v1, v160, v168
	v_add_f32_e32 v2, v162, v170
	v_add_f32_e32 v160, v164, v172
	v_add_f32_e32 v161, v166, v174
	s_nop 0
	v_permlane16_swap_b32_e32 v1, v160
	v_permlane16_swap_b32_e32 v2, v161
	v_add_f32_e32 v1, v1, v160
	v_add_f32_e32 v2, v2, v161
	v_cndmask_b32_e64 v160, v1, v2, s[4:5]
	v_cndmask_b32_e64 v1, v2, v1, s[4:5]
	s_bfe_u32 s14, s26, 0x4000a
	v_cmp_gt_u32_e32 vcc, s14, v180
	v_add_f32_dpp v1, v160, v1 row_ror:8 row_mask:0xf bank_mask:0xf bound_ctrl:1
	s_nop 1
	v_add_f32_dpp v1, v1, v1 row_half_mirror row_mask:0xf bank_mask:0xf bound_ctrl:1
	s_nop 1
	v_add_f32_dpp v2, v1, v1 quad_perm:[1,0,3,2] row_mask:0xf bank_mask:0xf bound_ctrl:1
	v_mov_b32_e32 v1, 0
	s_nop 0
	v_mov_b32_dpp v160, v2 quad_perm:[2,3,0,1] row_mask:0xf bank_mask:0xf bound_ctrl:1
	s_and_saveexec_b64 s[14:15], vcc
	s_cbranch_execz .Lp6a2_958
	s_and_b32 s26, s26, 0x3ff
	v_add_u32_e32 v1, s26, v180
	v_lshl_add_u32 v1, v1, 2, s85
	v_add_f32_e32 v2, v2, v160
	s_mov_b32 s26, 0x3e6d3388
	v_mul_f32_e32 v1, v2, v196
	v_fma_f32 v2, |v1|, s26, 1.0
	v_rcp_f32_e32 v2, v2
	v_mov_b32_e32 v160, 0xbf3a00e3
	v_cmp_gt_f32_e32 vcc, 0, v1
	v_fmamk_f32 v160, v2, 0x3f07dc22, v160
	v_fmaak_f32 v160, v2, v160, 0x3f35f0e3
	v_fmaak_f32 v160, v2, v160, 0xbe11a98e
	v_fmaak_f32 v160, v2, v160, 0x3e027906
	v_mul_f32_e32 v2, v2, v160
	v_mul_f32_e32 v160, v1, v1
	v_mul_f32_e32 v160, 0xbf38aa3b, v160
	v_exp_f32_e32 v160, v160
	s_nop 0
	v_mul_f32_e32 v2, v160, v2
	v_mul_f32_e32 v160, v1, v2
	v_fma_f32 v1, -v1, v2, v1
	v_cndmask_b32_e32 v1, v1, v160, vcc
	v_mul_f32_e32 v1, v201, v1
	ds_write_b32 v210, v1 offset:12288
.Lp6a2_958:
	s_or_b64 exec, exec, s[14:15]
	s_mov_b32 s26, s86
	s_mov_b32 s86, s27
	s_mov_b32 s27, s32
	s_mov_b32 s32, s37
	s_cmp_eq_u32 s22, s23
	s_cbranch_scc1 .Lp6_Adone
	s_branch .Lp6a0_top
.Lp6_Adone:
	s_waitcnt vmcnt(0)
	s_add_i32 s3, s22, -1
	s_min_i32 s2, s3, 0
	s_max_i32 s2, s2, 0
	s_lshl_b32 s2, s2, 2
	s_add_i32 s2, s85, s2
	v_mov_b32_e32 v1, s2
	ds_read_b32 v1, v1 offset:4864
	s_waitcnt lgkmcnt(0)
	v_readfirstlane_b32 s26, v1
	s_and_b32 s2, s26, 0x3ff
	s_bfe_u32 s3, s26, 0x4000a
	v_cmp_gt_u32_e32 vcc, s3, v182
	s_lshl_b32 s2, s2, 2
	s_add_i32 s2, s2, s85
	v_cndmask_b32_e32 v1, 0, v182, vcc
	v_lshl_add_u32 v1, v1, 2, s2
	ds_read_b32 v1, v1 offset:8192
	s_waitcnt lgkmcnt(0)
	v_lshlrev_b32_e32 v1, 10, v1
	v_and_b32_e32 v1, 0x3fffc00, v1
	s_nop 0
	v_readlane_b32 s44, v1, 0
	v_readlane_b32 s45, v1, 1
	v_readlane_b32 s46, v1, 2
	v_readlane_b32 s47, v1, 3
	v_readlane_b32 s48, v1, 4
	v_readlane_b32 s49, v1, 5
	v_readlane_b32 s50, v1, 6
	v_readlane_b32 s51, v1, 7
	s_nop 4
	buffer_load_dwordx4 v[68:71], v181, s[92:95], s44 offen
	buffer_load_dwordx4 v[64:67], v181, s[92:95], s45 offen
	buffer_load_dwordx4 v[60:63], v181, s[92:95], s46 offen
	buffer_load_dwordx4 v[56:59], v181, s[92:95], s47 offen
	buffer_load_dwordx4 v[48:51], v181, s[92:95], s48 offen
	buffer_load_dwordx4 v[32:35], v181, s[92:95], s49 offen
	buffer_load_dwordx4 v[16:19], v181, s[92:95], s50 offen
	buffer_load_dwordx4 v[12:15], v181, s[92:95], s51 offen
	s_add_i32 s3, s22, -1
	s_min_i32 s2, s3, 1
	s_max_i32 s2, s2, 0
	s_lshl_b32 s2, s2, 2
	s_add_i32 s2, s85, s2
	v_mov_b32_e32 v1, s2
	ds_read_b32 v1, v1 offset:4864
	s_waitcnt lgkmcnt(0)
	v_readfirstlane_b32 s86, v1
	s_and_b32 s2, s86, 0x3ff
	s_bfe_u32 s3, s86, 0x4000a
	v_cmp_gt_u32_e32 vcc, s3, v182
	s_lshl_b32 s2, s2, 2
	s_add_i32 s2, s2, s85
	v_cndmask_b32_e32 v1, 0, v182, vcc
	v_lshl_add_u32 v1, v1, 2, s2
	ds_read_b32 v1, v1 offset:8192
	s_waitcnt lgkmcnt(0)
	v_lshlrev_b32_e32 v1, 10, v1
	v_and_b32_e32 v1, 0x3fffc00, v1
	s_nop 0
	v_readlane_b32 s44, v1, 0
	v_readlane_b32 s45, v1, 1
	v_readlane_b32 s46, v1, 2
	v_readlane_b32 s47, v1, 3
	v_readlane_b32 s48, v1, 4
	v_readlane_b32 s49, v1, 5
	v_readlane_b32 s50, v1, 6
	v_readlane_b32 s51, v1, 7
	s_nop 4
	buffer_load_dwordx4 v[72:75], v181, s[92:95], s44 offen
	buffer_load_dwordx4 v[52:55], v181, s[92:95], s45 offen
	buffer_load_dwordx4 v[44:47], v181, s[92:95], s46 offen
	buffer_load_dwordx4 v[40:43], v181, s[92:95], s47 offen
	buffer_load_dwordx4 v[36:39], v181, s[92:95], s48 offen
	buffer_load_dwordx4 v[28:31], v181, s[92:95], s49 offen
	buffer_load_dwordx4 v[24:27], v181, s[92:95], s50 offen
	buffer_load_dwordx4 v[20:23], v181, s[92:95], s51 offen
	s_add_i32 s3, s22, -1
	s_min_i32 s2, s3, 2
	s_max_i32 s2, s2, 0
	s_lshl_b32 s2, s2, 2
	s_add_i32 s2, s85, s2
	v_mov_b32_e32 v1, s2
	ds_read_b32 v1, v1 offset:4864
	s_waitcnt lgkmcnt(0)
	v_readfirstlane_b32 s27, v1
	s_and_b32 s2, s27, 0x3ff
	s_bfe_u32 s3, s27, 0x4000a
	v_cmp_gt_u32_e32 vcc, s3, v182
	s_lshl_b32 s2, s2, 2
	s_add_i32 s2, s2, s85
	v_cndmask_b32_e32 v1, 0, v182, vcc
	v_lshl_add_u32 v1, v1, 2, s2
	ds_read_b32 v1, v1 offset:8192
	s_waitcnt lgkmcnt(0)
	v_lshlrev_b32_e32 v1, 10, v1
	v_and_b32_e32 v1, 0x3fffc00, v1
	s_nop 0
	v_readlane_b32 s44, v1, 0
	v_readlane_b32 s45, v1, 1
	v_readlane_b32 s46, v1, 2
	v_readlane_b32 s47, v1, 3
	v_readlane_b32 s48, v1, 4
	v_readlane_b32 s49, v1, 5
	v_readlane_b32 s50, v1, 6
	v_readlane_b32 s51, v1, 7
	s_nop 4
	buffer_load_dwordx4 v[224:227], v181, s[92:95], s44 offen
	buffer_load_dwordx4 v[228:231], v181, s[92:95], s45 offen
	buffer_load_dwordx4 v[232:235], v181, s[92:95], s46 offen
	buffer_load_dwordx4 v[236:239], v181, s[92:95], s47 offen
	buffer_load_dwordx4 v[240:243], v181, s[92:95], s48 offen
	buffer_load_dwordx4 v[244:247], v181, s[92:95], s49 offen
	buffer_load_dwordx4 v[248:251], v181, s[92:95], s50 offen
	buffer_load_dwordx4 v[216:219], v181, s[92:95], s51 offen
	s_add_i32 s3, s22, -1
	s_min_i32 s2, s3, 3
	s_max_i32 s2, s2, 0
	s_lshl_b32 s2, s2, 2
	s_add_i32 s2, s85, s2
	v_mov_b32_e32 v1, s2
	ds_read_b32 v1, v1 offset:4864
	s_waitcnt lgkmcnt(0)
	v_readfirstlane_b32 s32, v1
	s_mov_b32 s23, 0
.Lp6b0_top:
	s_add_i32 s23, s23, 1
	s_add_i32 s2, s23, 3
	s_add_i32 s3, s22, -1
	s_min_i32 s2, s2, s3
	s_lshl_b32 s2, s2, 2
	s_add_i32 s2, s85, s2
	v_mov_b32_e32 v1, s2
	ds_read_b32 v252, v1 offset:4864
	s_and_b32 s2, s32, 0x3ff
	s_bfe_u32 s3, s32, 0x4000a
	v_cmp_gt_u32_e32 vcc, s3, v182
	s_lshl_b32 s2, s2, 2
	s_add_i32 s2, s2, s85
	v_cndmask_b32_e32 v1, 0, v182, vcc
	v_lshl_add_u32 v1, v1, 2, s2
	ds_read_b32 v1, v1 offset:8192
	s_bfe_u32 s14, s26, 0x4000a
	v_cmp_gt_u32_e32 vcc, s14, v180
	v_mov_b32_e32 v2, 0
	s_and_b32 s2, s26, 0x3ff
	s_lshr_b32 s66, s26, 14
	s_and_saveexec_b64 s[14:15], vcc
	v_add_u32_e32 v210, s2, v180
	v_lshl_add_u32 v210, v210, 2, s85
	ds_read_b32 v2, v210 offset:12288
	s_or_b64 exec, exec, s[14:15]
	s_waitcnt vmcnt(16)
	s_waitcnt lgkmcnt(0)
	v_readfirstlane_b32 s37, v252
	v_lshlrev_b32_e32 v1, 10, v1
	v_and_b32_e32 v1, 0x3fffc00, v1
	s_nop 0
	v_readlane_b32 s44, v1, 0
	v_readlane_b32 s45, v1, 1
	v_readlane_b32 s46, v1, 2
	v_readlane_b32 s47, v1, 3
	v_readlane_b32 s48, v1, 4
	v_readlane_b32 s49, v1, 5
	v_readlane_b32 s50, v1, 6
	v_readlane_b32 s51, v1, 7
	v_mov_b32_e32 v1, v2
	s_bfe_u32 s36, s26, 0x4000a
	s_cmp_lt_i32 s66, 1
	s_cbranch_scc1 .Lp6b0_t0
	s_cmp_lt_i32 s66, 2
	s_cbranch_scc1 .Lp6b0_t1
	s_cmp_lg_u32 s66, 2
	s_cbranch_scc0 .Lp6b0_t2
	v_readlane_b32 s14, v1, 0
	v_cvt_pk_f32_fp8_e32 v[184:185], v68
	v_cvt_pk_f32_fp8_sdwa v[186:187], v68 src0_sel:WORD_1
	v_pk_fma_f32 v[78:79], v[184:185], s[14:15], v[78:79] op_sel_hi:[1,0,1]
	v_pk_fma_f32 v[80:81], v[186:187], s[14:15], v[80:81] op_sel_hi:[1,0,1]
	v_cvt_pk_f32_fp8_e32 v[188:189], v69
	v_cvt_pk_f32_fp8_sdwa v[190:191], v69 src0_sel:WORD_1
	v_pk_fma_f32 v[82:83], v[188:189], s[14:15], v[82:83] op_sel_hi:[1,0,1]
	v_pk_fma_f32 v[86:87], v[190:191], s[14:15], v[86:87] op_sel_hi:[1,0,1]
	v_cvt_pk_f32_fp8_e32 v[184:185], v70
	v_cvt_pk_f32_fp8_sdwa v[186:187], v70 src0_sel:WORD_1
	v_pk_fma_f32 v[88:89], v[184:185], s[14:15], v[88:89] op_sel_hi:[1,0,1]
	v_pk_fma_f32 v[90:91], v[186:187], s[14:15], v[90:91] op_sel_hi:[1,0,1]
	v_cvt_pk_f32_fp8_e32 v[188:189], v71
	v_cvt_pk_f32_fp8_sdwa v[190:191], v71 src0_sel:WORD_1
	v_pk_fma_f32 v[92:93], v[188:189], s[14:15], v[92:93] op_sel_hi:[1,0,1]
	v_pk_fma_f32 v[84:85], v[190:191], s[14:15], v[84:85] op_sel_hi:[1,0,1]
	v_readlane_b32 s14, v1, 8
	v_cvt_pk_f32_fp8_e32 v[184:185], v64
	v_cvt_pk_f32_fp8_sdwa v[186:187], v64 src0_sel:WORD_1
	v_pk_fma_f32 v[78:79], v[184:185], s[14:15], v[78:79] op_sel_hi:[1,0,1]
	v_pk_fma_f32 v[80:81], v[186:187], s[14:15], v[80:81] op_sel_hi:[1,0,1]
	v_cvt_pk_f32_fp8_e32 v[188:189], v65
	v_cvt_pk_f32_fp8_sdwa v[190:191], v65 src0_sel:WORD_1
	v_pk_fma_f32 v[82:83], v[188:189], s[14:15], v[82:83] op_sel_hi:[1,0,1]
	v_pk_fma_f32 v[86:87], v[190:191], s[14:15], v[86:87] op_sel_hi:[1,0,1]
	v_cvt_pk_f32_fp8_e32 v[184:185], v66
	v_cvt_pk_f32_fp8_sdwa v[186:187], v66 src0_sel:WORD_1
	v_pk_fma_f32 v[88:89], v[184:185], s[14:15], v[88:89] op_sel_hi:[1,0,1]
	v_pk_fma_f32 v[90:91], v[186:187], s[14:15], v[90:91] op_sel_hi:[1,0,1]
	v_cvt_pk_f32_fp8_e32 v[188:189], v67
	v_cvt_pk_f32_fp8_sdwa v[190:191], v67 src0_sel:WORD_1
	v_pk_fma_f32 v[92:93], v[188:189], s[14:15], v[92:93] op_sel_hi:[1,0,1]
	v_pk_fma_f32 v[84:85], v[190:191], s[14:15], v[84:85] op_sel_hi:[1,0,1]
	s_cmp_le_u32 s36, 2
	s_cbranch_scc1 .Lp6b0_axdone
	v_readlane_b32 s14, v1, 16
	v_cvt_pk_f32_fp8_e32 v[184:185], v60
	v_cvt_pk_f32_fp8_sdwa v[186:187], v60 src0_sel:WORD_1
	v_pk_fma_f32 v[78:79], v[184:185], s[14:15], v[78:79] op_sel_hi:[1,0,1]
	v_pk_fma_f32 v[80:81], v[186:187], s[14:15], v[80:81] op_sel_hi:[1,0,1]
	v_cvt_pk_f32_fp8_e32 v[188:189], v61
	v_cvt_pk_f32_fp8_sdwa v[190:191], v61 src0_sel:WORD_1
	v_pk_fma_f32 v[82:83], v[188:189], s[14:15], v[82:83] op_sel_hi:[1,0,1]
	v_pk_fma_f32 v[86:87], v[190:191], s[14:15], v[86:87] op_sel_hi:[1,0,1]
	v_cvt_pk_f32_fp8_e32 v[184:185], v62
	v_cvt_pk_f32_fp8_sdwa v[186:187], v62 src0_sel:WORD_1
	v_pk_fma_f32 v[88:89], v[184:185], s[14:15], v[88:89] op_sel_hi:[1,0,1]
	v_pk_fma_f32 v[90:91], v[186:187], s[14:15], v[90:91] op_sel_hi:[1,0,1]
	v_cvt_pk_f32_fp8_e32 v[188:189], v63
	v_cvt_pk_f32_fp8_sdwa v[190:191], v63 src0_sel:WORD_1
	v_pk_fma_f32 v[92:93], v[188:189], s[14:15], v[92:93] op_sel_hi:[1,0,1]
	v_pk_fma_f32 v[84:85], v[190:191], s[14:15], v[84:85] op_sel_hi:[1,0,1]
	v_readlane_b32 s14, v1, 24
	v_cvt_pk_f32_fp8_e32 v[184:185], v56
	v_cvt_pk_f32_fp8_sdwa v[186:187], v56 src0_sel:WORD_1
	v_pk_fma_f32 v[78:79], v[184:185], s[14:15], v[78:79] op_sel_hi:[1,0,1]
	v_pk_fma_f32 v[80:81], v[186:187], s[14:15], v[80:81] op_sel_hi:[1,0,1]
	v_cvt_pk_f32_fp8_e32 v[188:189], v57
	v_cvt_pk_f32_fp8_sdwa v[190:191], v57 src0_sel:WORD_1
	v_pk_fma_f32 v[82:83], v[188:189], s[14:15], v[82:83] op_sel_hi:[1,0,1]
	v_pk_fma_f32 v[86:87], v[190:191], s[14:15], v[86:87] op_sel_hi:[1,0,1]
	v_cvt_pk_f32_fp8_e32 v[184:185], v58
	v_cvt_pk_f32_fp8_sdwa v[186:187], v58 src0_sel:WORD_1
	v_pk_fma_f32 v[88:89], v[184:185], s[14:15], v[88:89] op_sel_hi:[1,0,1]
	v_pk_fma_f32 v[90:91], v[186:187], s[14:15], v[90:91] op_sel_hi:[1,0,1]
	v_cvt_pk_f32_fp8_e32 v[188:189], v59
	v_cvt_pk_f32_fp8_sdwa v[190:191], v59 src0_sel:WORD_1
	v_pk_fma_f32 v[92:93], v[188:189], s[14:15], v[92:93] op_sel_hi:[1,0,1]
	v_pk_fma_f32 v[84:85], v[190:191], s[14:15], v[84:85] op_sel_hi:[1,0,1]
	s_cmp_le_u32 s36, 4
	s_cbranch_scc1 .Lp6b0_axdone
	v_readlane_b32 s14, v1, 32
	v_cvt_pk_f32_fp8_e32 v[184:185], v48
	v_cvt_pk_f32_fp8_sdwa v[186:187], v48 src0_sel:WORD_1
	v_pk_fma_f32 v[78:79], v[184:185], s[14:15], v[78:79] op_sel_hi:[1,0,1]
	v_pk_fma_f32 v[80:81], v[186:187], s[14:15], v[80:81] op_sel_hi:[1,0,1]
	v_cvt_pk_f32_fp8_e32 v[188:189], v49
	v_cvt_pk_f32_fp8_sdwa v[190:191], v49 src0_sel:WORD_1
	v_pk_fma_f32 v[82:83], v[188:189], s[14:15], v[82:83] op_sel_hi:[1,0,1]
	v_pk_fma_f32 v[86:87], v[190:191], s[14:15], v[86:87] op_sel_hi:[1,0,1]
	v_cvt_pk_f32_fp8_e32 v[184:185], v50
	v_cvt_pk_f32_fp8_sdwa v[186:187], v50 src0_sel:WORD_1
	v_pk_fma_f32 v[88:89], v[184:185], s[14:15], v[88:89] op_sel_hi:[1,0,1]
	v_pk_fma_f32 v[90:91], v[186:187], s[14:15], v[90:91] op_sel_hi:[1,0,1]
	v_cvt_pk_f32_fp8_e32 v[188:189], v51
	v_cvt_pk_f32_fp8_sdwa v[190:191], v51 src0_sel:WORD_1
	v_pk_fma_f32 v[92:93], v[188:189], s[14:15], v[92:93] op_sel_hi:[1,0,1]
	v_pk_fma_f32 v[84:85], v[190:191], s[14:15], v[84:85] op_sel_hi:[1,0,1]
	v_readlane_b32 s14, v1, 40
	v_cvt_pk_f32_fp8_e32 v[184:185], v32
	v_cvt_pk_f32_fp8_sdwa v[186:187], v32 src0_sel:WORD_1
	v_pk_fma_f32 v[78:79], v[184:185], s[14:15], v[78:79] op_sel_hi:[1,0,1]
	v_pk_fma_f32 v[80:81], v[186:187], s[14:15], v[80:81] op_sel_hi:[1,0,1]
	v_cvt_pk_f32_fp8_e32 v[188:189], v33
	v_cvt_pk_f32_fp8_sdwa v[190:191], v33 src0_sel:WORD_1
	v_pk_fma_f32 v[82:83], v[188:189], s[14:15], v[82:83] op_sel_hi:[1,0,1]
	v_pk_fma_f32 v[86:87], v[190:191], s[14:15], v[86:87] op_sel_hi:[1,0,1]
	v_cvt_pk_f32_fp8_e32 v[184:185], v34
	v_cvt_pk_f32_fp8_sdwa v[186:187], v34 src0_sel:WORD_1
	v_pk_fma_f32 v[88:89], v[184:185], s[14:15], v[88:89] op_sel_hi:[1,0,1]
	v_pk_fma_f32 v[90:91], v[186:187], s[14:15], v[90:91] op_sel_hi:[1,0,1]
	v_cvt_pk_f32_fp8_e32 v[188:189], v35
	v_cvt_pk_f32_fp8_sdwa v[190:191], v35 src0_sel:WORD_1
	v_pk_fma_f32 v[92:93], v[188:189], s[14:15], v[92:93] op_sel_hi:[1,0,1]
	v_pk_fma_f32 v[84:85], v[190:191], s[14:15], v[84:85] op_sel_hi:[1,0,1]
	s_cmp_le_u32 s36, 6
	s_cbranch_scc1 .Lp6b0_axdone
	v_readlane_b32 s14, v1, 48
	v_cvt_pk_f32_fp8_e32 v[184:185], v16
	v_cvt_pk_f32_fp8_sdwa v[186:187], v16 src0_sel:WORD_1
	v_pk_fma_f32 v[78:79], v[184:185], s[14:15], v[78:79] op_sel_hi:[1,0,1]
	v_pk_fma_f32 v[80:81], v[186:187], s[14:15], v[80:81] op_sel_hi:[1,0,1]
	v_cvt_pk_f32_fp8_e32 v[188:189], v17
	v_cvt_pk_f32_fp8_sdwa v[190:191], v17 src0_sel:WORD_1
	v_pk_fma_f32 v[82:83], v[188:189], s[14:15], v[82:83] op_sel_hi:[1,0,1]
	v_pk_fma_f32 v[86:87], v[190:191], s[14:15], v[86:87] op_sel_hi:[1,0,1]
	v_cvt_pk_f32_fp8_e32 v[184:185], v18
	v_cvt_pk_f32_fp8_sdwa v[186:187], v18 src0_sel:WORD_1
	v_pk_fma_f32 v[88:89], v[184:185], s[14:15], v[88:89] op_sel_hi:[1,0,1]
	v_pk_fma_f32 v[90:91], v[186:187], s[14:15], v[90:91] op_sel_hi:[1,0,1]
	v_cvt_pk_f32_fp8_e32 v[188:189], v19
	v_cvt_pk_f32_fp8_sdwa v[190:191], v19 src0_sel:WORD_1
	v_pk_fma_f32 v[92:93], v[188:189], s[14:15], v[92:93] op_sel_hi:[1,0,1]
	v_pk_fma_f32 v[84:85], v[190:191], s[14:15], v[84:85] op_sel_hi:[1,0,1]
	v_readlane_b32 s14, v1, 56
	v_cvt_pk_f32_fp8_e32 v[184:185], v12
	v_cvt_pk_f32_fp8_sdwa v[186:187], v12 src0_sel:WORD_1
	v_pk_fma_f32 v[78:79], v[184:185], s[14:15], v[78:79] op_sel_hi:[1,0,1]
	v_pk_fma_f32 v[80:81], v[186:187], s[14:15], v[80:81] op_sel_hi:[1,0,1]
	v_cvt_pk_f32_fp8_e32 v[188:189], v13
	v_cvt_pk_f32_fp8_sdwa v[190:191], v13 src0_sel:WORD_1
	v_pk_fma_f32 v[82:83], v[188:189], s[14:15], v[82:83] op_sel_hi:[1,0,1]
	v_pk_fma_f32 v[86:87], v[190:191], s[14:15], v[86:87] op_sel_hi:[1,0,1]
	v_cvt_pk_f32_fp8_e32 v[184:185], v14
	v_cvt_pk_f32_fp8_sdwa v[186:187], v14 src0_sel:WORD_1
	v_pk_fma_f32 v[88:89], v[184:185], s[14:15], v[88:89] op_sel_hi:[1,0,1]
	v_pk_fma_f32 v[90:91], v[186:187], s[14:15], v[90:91] op_sel_hi:[1,0,1]
	v_cvt_pk_f32_fp8_e32 v[188:189], v15
	v_cvt_pk_f32_fp8_sdwa v[190:191], v15 src0_sel:WORD_1
	v_pk_fma_f32 v[92:93], v[188:189], s[14:15], v[92:93] op_sel_hi:[1,0,1]
	v_pk_fma_f32 v[84:85], v[190:191], s[14:15], v[84:85] op_sel_hi:[1,0,1]
	s_branch .Lp6b0_axdone

.Lp6b0_axdone:
	s_nop 4
	buffer_load_dwordx4 v[68:71], v181, s[92:95], s44 offen
	buffer_load_dwordx4 v[64:67], v181, s[92:95], s45 offen
	buffer_load_dwordx4 v[60:63], v181, s[92:95], s46 offen
	buffer_load_dwordx4 v[56:59], v181, s[92:95], s47 offen
	buffer_load_dwordx4 v[48:51], v181, s[92:95], s48 offen
	buffer_load_dwordx4 v[32:35], v181, s[92:95], s49 offen
	buffer_load_dwordx4 v[16:19], v181, s[92:95], s50 offen
	buffer_load_dwordx4 v[12:15], v181, s[92:95], s51 offen
	s_mov_b32 s26, s86
	s_mov_b32 s86, s27
	s_mov_b32 s27, s32
	s_mov_b32 s32, s37
	s_cmp_eq_u32 s22, s23
	s_cbranch_scc1 .LBB0_973
.Lp6b1_top:
	s_add_i32 s23, s23, 1
	s_add_i32 s2, s23, 3
	s_add_i32 s3, s22, -1
	s_min_i32 s2, s2, s3
	s_lshl_b32 s2, s2, 2
	s_add_i32 s2, s85, s2
	v_mov_b32_e32 v1, s2
	ds_read_b32 v252, v1 offset:4864
	s_and_b32 s2, s32, 0x3ff
	s_bfe_u32 s3, s32, 0x4000a
	v_cmp_gt_u32_e32 vcc, s3, v182
	s_lshl_b32 s2, s2, 2
	s_add_i32 s2, s2, s85
	v_cndmask_b32_e32 v1, 0, v182, vcc
	v_lshl_add_u32 v1, v1, 2, s2
	ds_read_b32 v1, v1 offset:8192
	s_bfe_u32 s14, s26, 0x4000a
	v_cmp_gt_u32_e32 vcc, s14, v180
	v_mov_b32_e32 v2, 0
	s_and_b32 s2, s26, 0x3ff
	s_lshr_b32 s66, s26, 14
	s_and_saveexec_b64 s[14:15], vcc
	v_add_u32_e32 v210, s2, v180
	v_lshl_add_u32 v210, v210, 2, s85
	ds_read_b32 v2, v210 offset:12288
	s_or_b64 exec, exec, s[14:15]
	s_waitcnt vmcnt(16)
	s_waitcnt lgkmcnt(0)
	v_readfirstlane_b32 s37, v252
	v_lshlrev_b32_e32 v1, 10, v1
	v_and_b32_e32 v1, 0x3fffc00, v1
	s_nop 0
	v_readlane_b32 s44, v1, 0
	v_readlane_b32 s45, v1, 1
	v_readlane_b32 s46, v1, 2
	v_readlane_b32 s47, v1, 3
	v_readlane_b32 s48, v1, 4
	v_readlane_b32 s49, v1, 5
	v_readlane_b32 s50, v1, 6
	v_readlane_b32 s51, v1, 7
	v_mov_b32_e32 v1, v2
	s_bfe_u32 s36, s26, 0x4000a
	s_cmp_lt_i32 s66, 1
	s_cbranch_scc1 .Lp6b1_t0
	s_cmp_lt_i32 s66, 2
	s_cbranch_scc1 .Lp6b1_t1
	s_cmp_lg_u32 s66, 2
	s_cbranch_scc0 .Lp6b1_t2
	v_readlane_b32 s14, v1, 0
	v_cvt_pk_f32_fp8_e32 v[184:185], v72
	v_cvt_pk_f32_fp8_sdwa v[186:187], v72 src0_sel:WORD_1
	v_pk_fma_f32 v[78:79], v[184:185], s[14:15], v[78:79] op_sel_hi:[1,0,1]
	v_pk_fma_f32 v[80:81], v[186:187], s[14:15], v[80:81] op_sel_hi:[1,0,1]
	v_cvt_pk_f32_fp8_e32 v[188:189], v73
	v_cvt_pk_f32_fp8_sdwa v[190:191], v73 src0_sel:WORD_1
	v_pk_fma_f32 v[82:83], v[188:189], s[14:15], v[82:83] op_sel_hi:[1,0,1]
	v_pk_fma_f32 v[86:87], v[190:191], s[14:15], v[86:87] op_sel_hi:[1,0,1]
	v_cvt_pk_f32_fp8_e32 v[184:185], v74
	v_cvt_pk_f32_fp8_sdwa v[186:187], v74 src0_sel:WORD_1
	v_pk_fma_f32 v[88:89], v[184:185], s[14:15], v[88:89] op_sel_hi:[1,0,1]
	v_pk_fma_f32 v[90:91], v[186:187], s[14:15], v[90:91] op_sel_hi:[1,0,1]
	v_cvt_pk_f32_fp8_e32 v[188:189], v75
	v_cvt_pk_f32_fp8_sdwa v[190:191], v75 src0_sel:WORD_1
	v_pk_fma_f32 v[92:93], v[188:189], s[14:15], v[92:93] op_sel_hi:[1,0,1]
	v_pk_fma_f32 v[84:85], v[190:191], s[14:15], v[84:85] op_sel_hi:[1,0,1]
	v_readlane_b32 s14, v1, 8
	v_cvt_pk_f32_fp8_e32 v[184:185], v52
	v_cvt_pk_f32_fp8_sdwa v[186:187], v52 src0_sel:WORD_1
	v_pk_fma_f32 v[78:79], v[184:185], s[14:15], v[78:79] op_sel_hi:[1,0,1]
	v_pk_fma_f32 v[80:81], v[186:187], s[14:15], v[80:81] op_sel_hi:[1,0,1]
	v_cvt_pk_f32_fp8_e32 v[188:189], v53
	v_cvt_pk_f32_fp8_sdwa v[190:191], v53 src0_sel:WORD_1
	v_pk_fma_f32 v[82:83], v[188:189], s[14:15], v[82:83] op_sel_hi:[1,0,1]
	v_pk_fma_f32 v[86:87], v[190:191], s[14:15], v[86:87] op_sel_hi:[1,0,1]
	v_cvt_pk_f32_fp8_e32 v[184:185], v54
	v_cvt_pk_f32_fp8_sdwa v[186:187], v54 src0_sel:WORD_1
	v_pk_fma_f32 v[88:89], v[184:185], s[14:15], v[88:89] op_sel_hi:[1,0,1]
	v_pk_fma_f32 v[90:91], v[186:187], s[14:15], v[90:91] op_sel_hi:[1,0,1]
	v_cvt_pk_f32_fp8_e32 v[188:189], v55
	v_cvt_pk_f32_fp8_sdwa v[190:191], v55 src0_sel:WORD_1
	v_pk_fma_f32 v[92:93], v[188:189], s[14:15], v[92:93] op_sel_hi:[1,0,1]
	v_pk_fma_f32 v[84:85], v[190:191], s[14:15], v[84:85] op_sel_hi:[1,0,1]
	s_cmp_le_u32 s36, 2
	s_cbranch_scc1 .Lp6b1_axdone
	v_readlane_b32 s14, v1, 16
	v_cvt_pk_f32_fp8_e32 v[184:185], v44
	v_cvt_pk_f32_fp8_sdwa v[186:187], v44 src0_sel:WORD_1
	v_pk_fma_f32 v[78:79], v[184:185], s[14:15], v[78:79] op_sel_hi:[1,0,1]
	v_pk_fma_f32 v[80:81], v[186:187], s[14:15], v[80:81] op_sel_hi:[1,0,1]
	v_cvt_pk_f32_fp8_e32 v[188:189], v45
	v_cvt_pk_f32_fp8_sdwa v[190:191], v45 src0_sel:WORD_1
	v_pk_fma_f32 v[82:83], v[188:189], s[14:15], v[82:83] op_sel_hi:[1,0,1]
	v_pk_fma_f32 v[86:87], v[190:191], s[14:15], v[86:87] op_sel_hi:[1,0,1]
	v_cvt_pk_f32_fp8_e32 v[184:185], v46
	v_cvt_pk_f32_fp8_sdwa v[186:187], v46 src0_sel:WORD_1
	v_pk_fma_f32 v[88:89], v[184:185], s[14:15], v[88:89] op_sel_hi:[1,0,1]
	v_pk_fma_f32 v[90:91], v[186:187], s[14:15], v[90:91] op_sel_hi:[1,0,1]
	v_cvt_pk_f32_fp8_e32 v[188:189], v47
	v_cvt_pk_f32_fp8_sdwa v[190:191], v47 src0_sel:WORD_1
	v_pk_fma_f32 v[92:93], v[188:189], s[14:15], v[92:93] op_sel_hi:[1,0,1]
	v_pk_fma_f32 v[84:85], v[190:191], s[14:15], v[84:85] op_sel_hi:[1,0,1]
	v_readlane_b32 s14, v1, 24
	v_cvt_pk_f32_fp8_e32 v[184:185], v40
	v_cvt_pk_f32_fp8_sdwa v[186:187], v40 src0_sel:WORD_1
	v_pk_fma_f32 v[78:79], v[184:185], s[14:15], v[78:79] op_sel_hi:[1,0,1]
	v_pk_fma_f32 v[80:81], v[186:187], s[14:15], v[80:81] op_sel_hi:[1,0,1]
	v_cvt_pk_f32_fp8_e32 v[188:189], v41
	v_cvt_pk_f32_fp8_sdwa v[190:191], v41 src0_sel:WORD_1
	v_pk_fma_f32 v[82:83], v[188:189], s[14:15], v[82:83] op_sel_hi:[1,0,1]
	v_pk_fma_f32 v[86:87], v[190:191], s[14:15], v[86:87] op_sel_hi:[1,0,1]
	v_cvt_pk_f32_fp8_e32 v[184:185], v42
	v_cvt_pk_f32_fp8_sdwa v[186:187], v42 src0_sel:WORD_1
	v_pk_fma_f32 v[88:89], v[184:185], s[14:15], v[88:89] op_sel_hi:[1,0,1]
	v_pk_fma_f32 v[90:91], v[186:187], s[14:15], v[90:91] op_sel_hi:[1,0,1]
	v_cvt_pk_f32_fp8_e32 v[188:189], v43
	v_cvt_pk_f32_fp8_sdwa v[190:191], v43 src0_sel:WORD_1
	v_pk_fma_f32 v[92:93], v[188:189], s[14:15], v[92:93] op_sel_hi:[1,0,1]
	v_pk_fma_f32 v[84:85], v[190:191], s[14:15], v[84:85] op_sel_hi:[1,0,1]
	s_cmp_le_u32 s36, 4
	s_cbranch_scc1 .Lp6b1_axdone
	v_readlane_b32 s14, v1, 32
	v_cvt_pk_f32_fp8_e32 v[184:185], v36
	v_cvt_pk_f32_fp8_sdwa v[186:187], v36 src0_sel:WORD_1
	v_pk_fma_f32 v[78:79], v[184:185], s[14:15], v[78:79] op_sel_hi:[1,0,1]
	v_pk_fma_f32 v[80:81], v[186:187], s[14:15], v[80:81] op_sel_hi:[1,0,1]
	v_cvt_pk_f32_fp8_e32 v[188:189], v37
	v_cvt_pk_f32_fp8_sdwa v[190:191], v37 src0_sel:WORD_1
	v_pk_fma_f32 v[82:83], v[188:189], s[14:15], v[82:83] op_sel_hi:[1,0,1]
	v_pk_fma_f32 v[86:87], v[190:191], s[14:15], v[86:87] op_sel_hi:[1,0,1]
	v_cvt_pk_f32_fp8_e32 v[184:185], v38
	v_cvt_pk_f32_fp8_sdwa v[186:187], v38 src0_sel:WORD_1
	v_pk_fma_f32 v[88:89], v[184:185], s[14:15], v[88:89] op_sel_hi:[1,0,1]
	v_pk_fma_f32 v[90:91], v[186:187], s[14:15], v[90:91] op_sel_hi:[1,0,1]
	v_cvt_pk_f32_fp8_e32 v[188:189], v39
	v_cvt_pk_f32_fp8_sdwa v[190:191], v39 src0_sel:WORD_1
	v_pk_fma_f32 v[92:93], v[188:189], s[14:15], v[92:93] op_sel_hi:[1,0,1]
	v_pk_fma_f32 v[84:85], v[190:191], s[14:15], v[84:85] op_sel_hi:[1,0,1]
	v_readlane_b32 s14, v1, 40
	v_cvt_pk_f32_fp8_e32 v[184:185], v28
	v_cvt_pk_f32_fp8_sdwa v[186:187], v28 src0_sel:WORD_1
	v_pk_fma_f32 v[78:79], v[184:185], s[14:15], v[78:79] op_sel_hi:[1,0,1]
	v_pk_fma_f32 v[80:81], v[186:187], s[14:15], v[80:81] op_sel_hi:[1,0,1]
	v_cvt_pk_f32_fp8_e32 v[188:189], v29
	v_cvt_pk_f32_fp8_sdwa v[190:191], v29 src0_sel:WORD_1
	v_pk_fma_f32 v[82:83], v[188:189], s[14:15], v[82:83] op_sel_hi:[1,0,1]
	v_pk_fma_f32 v[86:87], v[190:191], s[14:15], v[86:87] op_sel_hi:[1,0,1]
	v_cvt_pk_f32_fp8_e32 v[184:185], v30
	v_cvt_pk_f32_fp8_sdwa v[186:187], v30 src0_sel:WORD_1
	v_pk_fma_f32 v[88:89], v[184:185], s[14:15], v[88:89] op_sel_hi:[1,0,1]
	v_pk_fma_f32 v[90:91], v[186:187], s[14:15], v[90:91] op_sel_hi:[1,0,1]
	v_cvt_pk_f32_fp8_e32 v[188:189], v31
	v_cvt_pk_f32_fp8_sdwa v[190:191], v31 src0_sel:WORD_1
	v_pk_fma_f32 v[92:93], v[188:189], s[14:15], v[92:93] op_sel_hi:[1,0,1]
	v_pk_fma_f32 v[84:85], v[190:191], s[14:15], v[84:85] op_sel_hi:[1,0,1]
	s_cmp_le_u32 s36, 6
	s_cbranch_scc1 .Lp6b1_axdone
	v_readlane_b32 s14, v1, 48
	v_cvt_pk_f32_fp8_e32 v[184:185], v24
	v_cvt_pk_f32_fp8_sdwa v[186:187], v24 src0_sel:WORD_1
	v_pk_fma_f32 v[78:79], v[184:185], s[14:15], v[78:79] op_sel_hi:[1,0,1]
	v_pk_fma_f32 v[80:81], v[186:187], s[14:15], v[80:81] op_sel_hi:[1,0,1]
	v_cvt_pk_f32_fp8_e32 v[188:189], v25
	v_cvt_pk_f32_fp8_sdwa v[190:191], v25 src0_sel:WORD_1
	v_pk_fma_f32 v[82:83], v[188:189], s[14:15], v[82:83] op_sel_hi:[1,0,1]
	v_pk_fma_f32 v[86:87], v[190:191], s[14:15], v[86:87] op_sel_hi:[1,0,1]
	v_cvt_pk_f32_fp8_e32 v[184:185], v26
	v_cvt_pk_f32_fp8_sdwa v[186:187], v26 src0_sel:WORD_1
	v_pk_fma_f32 v[88:89], v[184:185], s[14:15], v[88:89] op_sel_hi:[1,0,1]
	v_pk_fma_f32 v[90:91], v[186:187], s[14:15], v[90:91] op_sel_hi:[1,0,1]
	v_cvt_pk_f32_fp8_e32 v[188:189], v27
	v_cvt_pk_f32_fp8_sdwa v[190:191], v27 src0_sel:WORD_1
	v_pk_fma_f32 v[92:93], v[188:189], s[14:15], v[92:93] op_sel_hi:[1,0,1]
	v_pk_fma_f32 v[84:85], v[190:191], s[14:15], v[84:85] op_sel_hi:[1,0,1]
	v_readlane_b32 s14, v1, 56
	v_cvt_pk_f32_fp8_e32 v[184:185], v20
	v_cvt_pk_f32_fp8_sdwa v[186:187], v20 src0_sel:WORD_1
	v_pk_fma_f32 v[78:79], v[184:185], s[14:15], v[78:79] op_sel_hi:[1,0,1]
	v_pk_fma_f32 v[80:81], v[186:187], s[14:15], v[80:81] op_sel_hi:[1,0,1]
	v_cvt_pk_f32_fp8_e32 v[188:189], v21
	v_cvt_pk_f32_fp8_sdwa v[190:191], v21 src0_sel:WORD_1
	v_pk_fma_f32 v[82:83], v[188:189], s[14:15], v[82:83] op_sel_hi:[1,0,1]
	v_pk_fma_f32 v[86:87], v[190:191], s[14:15], v[86:87] op_sel_hi:[1,0,1]
	v_cvt_pk_f32_fp8_e32 v[184:185], v22
	v_cvt_pk_f32_fp8_sdwa v[186:187], v22 src0_sel:WORD_1
	v_pk_fma_f32 v[88:89], v[184:185], s[14:15], v[88:89] op_sel_hi:[1,0,1]
	v_pk_fma_f32 v[90:91], v[186:187], s[14:15], v[90:91] op_sel_hi:[1,0,1]
	v_cvt_pk_f32_fp8_e32 v[188:189], v23
	v_cvt_pk_f32_fp8_sdwa v[190:191], v23 src0_sel:WORD_1
	v_pk_fma_f32 v[92:93], v[188:189], s[14:15], v[92:93] op_sel_hi:[1,0,1]
	v_pk_fma_f32 v[84:85], v[190:191], s[14:15], v[84:85] op_sel_hi:[1,0,1]
	s_branch .Lp6b1_axdone

.Lp6b1_axdone:
	s_nop 4
	buffer_load_dwordx4 v[72:75], v181, s[92:95], s44 offen
	buffer_load_dwordx4 v[52:55], v181, s[92:95], s45 offen
	buffer_load_dwordx4 v[44:47], v181, s[92:95], s46 offen
	buffer_load_dwordx4 v[40:43], v181, s[92:95], s47 offen
	buffer_load_dwordx4 v[36:39], v181, s[92:95], s48 offen
	buffer_load_dwordx4 v[28:31], v181, s[92:95], s49 offen
	buffer_load_dwordx4 v[24:27], v181, s[92:95], s50 offen
	buffer_load_dwordx4 v[20:23], v181, s[92:95], s51 offen
	s_mov_b32 s26, s86
	s_mov_b32 s86, s27
	s_mov_b32 s27, s32
	s_mov_b32 s32, s37
	s_cmp_eq_u32 s22, s23
	s_cbranch_scc1 .LBB0_973
.Lp6b2_top:
	s_add_i32 s23, s23, 1
	s_add_i32 s2, s23, 3
	s_add_i32 s3, s22, -1
	s_min_i32 s2, s2, s3
	s_lshl_b32 s2, s2, 2
	s_add_i32 s2, s85, s2
	v_mov_b32_e32 v1, s2
	ds_read_b32 v252, v1 offset:4864
	s_and_b32 s2, s32, 0x3ff
	s_bfe_u32 s3, s32, 0x4000a
	v_cmp_gt_u32_e32 vcc, s3, v182
	s_lshl_b32 s2, s2, 2
	s_add_i32 s2, s2, s85
	v_cndmask_b32_e32 v1, 0, v182, vcc
	v_lshl_add_u32 v1, v1, 2, s2
	ds_read_b32 v1, v1 offset:8192
	s_bfe_u32 s14, s26, 0x4000a
	v_cmp_gt_u32_e32 vcc, s14, v180
	v_mov_b32_e32 v2, 0
	s_and_b32 s2, s26, 0x3ff
	s_lshr_b32 s66, s26, 14
	s_and_saveexec_b64 s[14:15], vcc
	v_add_u32_e32 v210, s2, v180
	v_lshl_add_u32 v210, v210, 2, s85
	ds_read_b32 v2, v210 offset:12288
	s_or_b64 exec, exec, s[14:15]
	s_waitcnt vmcnt(16)
	s_waitcnt lgkmcnt(0)
	v_readfirstlane_b32 s37, v252
	v_lshlrev_b32_e32 v1, 10, v1
	v_and_b32_e32 v1, 0x3fffc00, v1
	s_nop 0
	v_readlane_b32 s44, v1, 0
	v_readlane_b32 s45, v1, 1
	v_readlane_b32 s46, v1, 2
	v_readlane_b32 s47, v1, 3
	v_readlane_b32 s48, v1, 4
	v_readlane_b32 s49, v1, 5
	v_readlane_b32 s50, v1, 6
	v_readlane_b32 s51, v1, 7
	v_mov_b32_e32 v1, v2
	s_bfe_u32 s36, s26, 0x4000a
	s_cmp_lt_i32 s66, 1
	s_cbranch_scc1 .Lp6b2_t0
	s_cmp_lt_i32 s66, 2
	s_cbranch_scc1 .Lp6b2_t1
	s_cmp_lg_u32 s66, 2
	s_cbranch_scc0 .Lp6b2_t2
	v_readlane_b32 s14, v1, 0
	v_cvt_pk_f32_fp8_e32 v[184:185], v224
	v_cvt_pk_f32_fp8_sdwa v[186:187], v224 src0_sel:WORD_1
	v_pk_fma_f32 v[78:79], v[184:185], s[14:15], v[78:79] op_sel_hi:[1,0,1]
	v_pk_fma_f32 v[80:81], v[186:187], s[14:15], v[80:81] op_sel_hi:[1,0,1]
	v_cvt_pk_f32_fp8_e32 v[188:189], v225
	v_cvt_pk_f32_fp8_sdwa v[190:191], v225 src0_sel:WORD_1
	v_pk_fma_f32 v[82:83], v[188:189], s[14:15], v[82:83] op_sel_hi:[1,0,1]
	v_pk_fma_f32 v[86:87], v[190:191], s[14:15], v[86:87] op_sel_hi:[1,0,1]
	v_cvt_pk_f32_fp8_e32 v[184:185], v226
	v_cvt_pk_f32_fp8_sdwa v[186:187], v226 src0_sel:WORD_1
	v_pk_fma_f32 v[88:89], v[184:185], s[14:15], v[88:89] op_sel_hi:[1,0,1]
	v_pk_fma_f32 v[90:91], v[186:187], s[14:15], v[90:91] op_sel_hi:[1,0,1]
	v_cvt_pk_f32_fp8_e32 v[188:189], v227
	v_cvt_pk_f32_fp8_sdwa v[190:191], v227 src0_sel:WORD_1
	v_pk_fma_f32 v[92:93], v[188:189], s[14:15], v[92:93] op_sel_hi:[1,0,1]
	v_pk_fma_f32 v[84:85], v[190:191], s[14:15], v[84:85] op_sel_hi:[1,0,1]
	v_readlane_b32 s14, v1, 8
	v_cvt_pk_f32_fp8_e32 v[184:185], v228
	v_cvt_pk_f32_fp8_sdwa v[186:187], v228 src0_sel:WORD_1
	v_pk_fma_f32 v[78:79], v[184:185], s[14:15], v[78:79] op_sel_hi:[1,0,1]
	v_pk_fma_f32 v[80:81], v[186:187], s[14:15], v[80:81] op_sel_hi:[1,0,1]
	v_cvt_pk_f32_fp8_e32 v[188:189], v229
	v_cvt_pk_f32_fp8_sdwa v[190:191], v229 src0_sel:WORD_1
	v_pk_fma_f32 v[82:83], v[188:189], s[14:15], v[82:83] op_sel_hi:[1,0,1]
	v_pk_fma_f32 v[86:87], v[190:191], s[14:15], v[86:87] op_sel_hi:[1,0,1]
	v_cvt_pk_f32_fp8_e32 v[184:185], v230
	v_cvt_pk_f32_fp8_sdwa v[186:187], v230 src0_sel:WORD_1
	v_pk_fma_f32 v[88:89], v[184:185], s[14:15], v[88:89] op_sel_hi:[1,0,1]
	v_pk_fma_f32 v[90:91], v[186:187], s[14:15], v[90:91] op_sel_hi:[1,0,1]
	v_cvt_pk_f32_fp8_e32 v[188:189], v231
	v_cvt_pk_f32_fp8_sdwa v[190:191], v231 src0_sel:WORD_1
	v_pk_fma_f32 v[92:93], v[188:189], s[14:15], v[92:93] op_sel_hi:[1,0,1]
	v_pk_fma_f32 v[84:85], v[190:191], s[14:15], v[84:85] op_sel_hi:[1,0,1]
	s_cmp_le_u32 s36, 2
	s_cbranch_scc1 .Lp6b2_axdone
	v_readlane_b32 s14, v1, 16
	v_cvt_pk_f32_fp8_e32 v[184:185], v232
	v_cvt_pk_f32_fp8_sdwa v[186:187], v232 src0_sel:WORD_1
	v_pk_fma_f32 v[78:79], v[184:185], s[14:15], v[78:79] op_sel_hi:[1,0,1]
	v_pk_fma_f32 v[80:81], v[186:187], s[14:15], v[80:81] op_sel_hi:[1,0,1]
	v_cvt_pk_f32_fp8_e32 v[188:189], v233
	v_cvt_pk_f32_fp8_sdwa v[190:191], v233 src0_sel:WORD_1
	v_pk_fma_f32 v[82:83], v[188:189], s[14:15], v[82:83] op_sel_hi:[1,0,1]
	v_pk_fma_f32 v[86:87], v[190:191], s[14:15], v[86:87] op_sel_hi:[1,0,1]
	v_cvt_pk_f32_fp8_e32 v[184:185], v234
	v_cvt_pk_f32_fp8_sdwa v[186:187], v234 src0_sel:WORD_1
	v_pk_fma_f32 v[88:89], v[184:185], s[14:15], v[88:89] op_sel_hi:[1,0,1]
	v_pk_fma_f32 v[90:91], v[186:187], s[14:15], v[90:91] op_sel_hi:[1,0,1]
	v_cvt_pk_f32_fp8_e32 v[188:189], v235
	v_cvt_pk_f32_fp8_sdwa v[190:191], v235 src0_sel:WORD_1
	v_pk_fma_f32 v[92:93], v[188:189], s[14:15], v[92:93] op_sel_hi:[1,0,1]
	v_pk_fma_f32 v[84:85], v[190:191], s[14:15], v[84:85] op_sel_hi:[1,0,1]
	v_readlane_b32 s14, v1, 24
	v_cvt_pk_f32_fp8_e32 v[184:185], v236
	v_cvt_pk_f32_fp8_sdwa v[186:187], v236 src0_sel:WORD_1
	v_pk_fma_f32 v[78:79], v[184:185], s[14:15], v[78:79] op_sel_hi:[1,0,1]
	v_pk_fma_f32 v[80:81], v[186:187], s[14:15], v[80:81] op_sel_hi:[1,0,1]
	v_cvt_pk_f32_fp8_e32 v[188:189], v237
	v_cvt_pk_f32_fp8_sdwa v[190:191], v237 src0_sel:WORD_1
	v_pk_fma_f32 v[82:83], v[188:189], s[14:15], v[82:83] op_sel_hi:[1,0,1]
	v_pk_fma_f32 v[86:87], v[190:191], s[14:15], v[86:87] op_sel_hi:[1,0,1]
	v_cvt_pk_f32_fp8_e32 v[184:185], v238
	v_cvt_pk_f32_fp8_sdwa v[186:187], v238 src0_sel:WORD_1
	v_pk_fma_f32 v[88:89], v[184:185], s[14:15], v[88:89] op_sel_hi:[1,0,1]
	v_pk_fma_f32 v[90:91], v[186:187], s[14:15], v[90:91] op_sel_hi:[1,0,1]
	v_cvt_pk_f32_fp8_e32 v[188:189], v239
	v_cvt_pk_f32_fp8_sdwa v[190:191], v239 src0_sel:WORD_1
	v_pk_fma_f32 v[92:93], v[188:189], s[14:15], v[92:93] op_sel_hi:[1,0,1]
	v_pk_fma_f32 v[84:85], v[190:191], s[14:15], v[84:85] op_sel_hi:[1,0,1]
	s_cmp_le_u32 s36, 4
	s_cbranch_scc1 .Lp6b2_axdone
	v_readlane_b32 s14, v1, 32
	v_cvt_pk_f32_fp8_e32 v[184:185], v240
	v_cvt_pk_f32_fp8_sdwa v[186:187], v240 src0_sel:WORD_1
	v_pk_fma_f32 v[78:79], v[184:185], s[14:15], v[78:79] op_sel_hi:[1,0,1]
	v_pk_fma_f32 v[80:81], v[186:187], s[14:15], v[80:81] op_sel_hi:[1,0,1]
	v_cvt_pk_f32_fp8_e32 v[188:189], v241
	v_cvt_pk_f32_fp8_sdwa v[190:191], v241 src0_sel:WORD_1
	v_pk_fma_f32 v[82:83], v[188:189], s[14:15], v[82:83] op_sel_hi:[1,0,1]
	v_pk_fma_f32 v[86:87], v[190:191], s[14:15], v[86:87] op_sel_hi:[1,0,1]
	v_cvt_pk_f32_fp8_e32 v[184:185], v242
	v_cvt_pk_f32_fp8_sdwa v[186:187], v242 src0_sel:WORD_1
	v_pk_fma_f32 v[88:89], v[184:185], s[14:15], v[88:89] op_sel_hi:[1,0,1]
	v_pk_fma_f32 v[90:91], v[186:187], s[14:15], v[90:91] op_sel_hi:[1,0,1]
	v_cvt_pk_f32_fp8_e32 v[188:189], v243
	v_cvt_pk_f32_fp8_sdwa v[190:191], v243 src0_sel:WORD_1
	v_pk_fma_f32 v[92:93], v[188:189], s[14:15], v[92:93] op_sel_hi:[1,0,1]
	v_pk_fma_f32 v[84:85], v[190:191], s[14:15], v[84:85] op_sel_hi:[1,0,1]
	v_readlane_b32 s14, v1, 40
	v_cvt_pk_f32_fp8_e32 v[184:185], v244
	v_cvt_pk_f32_fp8_sdwa v[186:187], v244 src0_sel:WORD_1
	v_pk_fma_f32 v[78:79], v[184:185], s[14:15], v[78:79] op_sel_hi:[1,0,1]
	v_pk_fma_f32 v[80:81], v[186:187], s[14:15], v[80:81] op_sel_hi:[1,0,1]
	v_cvt_pk_f32_fp8_e32 v[188:189], v245
	v_cvt_pk_f32_fp8_sdwa v[190:191], v245 src0_sel:WORD_1
	v_pk_fma_f32 v[82:83], v[188:189], s[14:15], v[82:83] op_sel_hi:[1,0,1]
	v_pk_fma_f32 v[86:87], v[190:191], s[14:15], v[86:87] op_sel_hi:[1,0,1]
	v_cvt_pk_f32_fp8_e32 v[184:185], v246
	v_cvt_pk_f32_fp8_sdwa v[186:187], v246 src0_sel:WORD_1
	v_pk_fma_f32 v[88:89], v[184:185], s[14:15], v[88:89] op_sel_hi:[1,0,1]
	v_pk_fma_f32 v[90:91], v[186:187], s[14:15], v[90:91] op_sel_hi:[1,0,1]
	v_cvt_pk_f32_fp8_e32 v[188:189], v247
	v_cvt_pk_f32_fp8_sdwa v[190:191], v247 src0_sel:WORD_1
	v_pk_fma_f32 v[92:93], v[188:189], s[14:15], v[92:93] op_sel_hi:[1,0,1]
	v_pk_fma_f32 v[84:85], v[190:191], s[14:15], v[84:85] op_sel_hi:[1,0,1]
	s_cmp_le_u32 s36, 6
	s_cbranch_scc1 .Lp6b2_axdone
	v_readlane_b32 s14, v1, 48
	v_cvt_pk_f32_fp8_e32 v[184:185], v248
	v_cvt_pk_f32_fp8_sdwa v[186:187], v248 src0_sel:WORD_1
	v_pk_fma_f32 v[78:79], v[184:185], s[14:15], v[78:79] op_sel_hi:[1,0,1]
	v_pk_fma_f32 v[80:81], v[186:187], s[14:15], v[80:81] op_sel_hi:[1,0,1]
	v_cvt_pk_f32_fp8_e32 v[188:189], v249
	v_cvt_pk_f32_fp8_sdwa v[190:191], v249 src0_sel:WORD_1
	v_pk_fma_f32 v[82:83], v[188:189], s[14:15], v[82:83] op_sel_hi:[1,0,1]
	v_pk_fma_f32 v[86:87], v[190:191], s[14:15], v[86:87] op_sel_hi:[1,0,1]
	v_cvt_pk_f32_fp8_e32 v[184:185], v250
	v_cvt_pk_f32_fp8_sdwa v[186:187], v250 src0_sel:WORD_1
	v_pk_fma_f32 v[88:89], v[184:185], s[14:15], v[88:89] op_sel_hi:[1,0,1]
	v_pk_fma_f32 v[90:91], v[186:187], s[14:15], v[90:91] op_sel_hi:[1,0,1]
	v_cvt_pk_f32_fp8_e32 v[188:189], v251
	v_cvt_pk_f32_fp8_sdwa v[190:191], v251 src0_sel:WORD_1
	v_pk_fma_f32 v[92:93], v[188:189], s[14:15], v[92:93] op_sel_hi:[1,0,1]
	v_pk_fma_f32 v[84:85], v[190:191], s[14:15], v[84:85] op_sel_hi:[1,0,1]
	v_readlane_b32 s14, v1, 56
	v_cvt_pk_f32_fp8_e32 v[184:185], v216
	v_cvt_pk_f32_fp8_sdwa v[186:187], v216 src0_sel:WORD_1
	v_pk_fma_f32 v[78:79], v[184:185], s[14:15], v[78:79] op_sel_hi:[1,0,1]
	v_pk_fma_f32 v[80:81], v[186:187], s[14:15], v[80:81] op_sel_hi:[1,0,1]
	v_cvt_pk_f32_fp8_e32 v[188:189], v217
	v_cvt_pk_f32_fp8_sdwa v[190:191], v217 src0_sel:WORD_1
	v_pk_fma_f32 v[82:83], v[188:189], s[14:15], v[82:83] op_sel_hi:[1,0,1]
	v_pk_fma_f32 v[86:87], v[190:191], s[14:15], v[86:87] op_sel_hi:[1,0,1]
	v_cvt_pk_f32_fp8_e32 v[184:185], v218
	v_cvt_pk_f32_fp8_sdwa v[186:187], v218 src0_sel:WORD_1
	v_pk_fma_f32 v[88:89], v[184:185], s[14:15], v[88:89] op_sel_hi:[1,0,1]
	v_pk_fma_f32 v[90:91], v[186:187], s[14:15], v[90:91] op_sel_hi:[1,0,1]
	v_cvt_pk_f32_fp8_e32 v[188:189], v219
	v_cvt_pk_f32_fp8_sdwa v[190:191], v219 src0_sel:WORD_1
	v_pk_fma_f32 v[92:93], v[188:189], s[14:15], v[92:93] op_sel_hi:[1,0,1]
	v_pk_fma_f32 v[84:85], v[190:191], s[14:15], v[84:85] op_sel_hi:[1,0,1]
	s_branch .Lp6b2_axdone

.Lp6b2_axdone:
	s_nop 4
	buffer_load_dwordx4 v[224:227], v181, s[92:95], s44 offen
	buffer_load_dwordx4 v[228:231], v181, s[92:95], s45 offen
	buffer_load_dwordx4 v[232:235], v181, s[92:95], s46 offen
	buffer_load_dwordx4 v[236:239], v181, s[92:95], s47 offen
	buffer_load_dwordx4 v[240:243], v181, s[92:95], s48 offen
	buffer_load_dwordx4 v[244:247], v181, s[92:95], s49 offen
	buffer_load_dwordx4 v[248:251], v181, s[92:95], s50 offen
	buffer_load_dwordx4 v[216:219], v181, s[92:95], s51 offen
	s_mov_b32 s26, s86
	s_mov_b32 s86, s27
	s_mov_b32 s27, s32
	s_mov_b32 s32, s37
	s_cmp_eq_u32 s22, s23
	s_cbranch_scc1 .LBB0_973
	s_branch .Lp6b0_top
